# speedup vs baseline: 1.0059x; 1.0037x over previous
_Z6gemm_gILi32ELi64ELi16ELi32ELi1ELi1ELi128ELi3EEv5GemmP:
	s_lshl_b32 s90, s3, 8
	s_add_u32 s90, s90, s2
	s_bfe_u32 s3, s90, 0x10003
	s_lshr_b32 s91, s90, 4
	s_lshl_b32 s91, s91, 3
	s_and_b32 s2, s90, 7
	s_or_b32 s2, s2, s91
	s_load_dwordx8 s[4:11], s[0:1], 0x0
	s_load_dwordx4 s[12:15], s[0:1], 0x38
	s_load_dwordx2 s[16:17], s[0:1], 0x68
	v_lshrrev_b32_e32 v7, 4, v0
	v_xor_b32_e32 v1, v7, v0
	s_waitcnt lgkmcnt(0)
	s_lshl_b32 s15, s2, 5
	v_lshlrev_b32_e32 v1, 3, v1
	v_and_b32_e32 v2, 0x78, v1
	v_or_b32_e32 v4, s15, v7
	v_bitop3_b32 v3, v7, 47, s15 bitop3:0xc8
	v_mad_u64_u32 v[4:5], s[18:19], v4, s13, v[2:3]
	v_or_b32_e32 v5, 0x100, v0
	v_lshrrev_b32_e32 v12, 4, v5
	v_xor_b32_e32 v5, v12, v0
	v_lshlrev_b32_e32 v5, 3, v5
	s_bfe_u32 s20, s2, 0x60001
	v_and_b32_e32 v6, 0x78, v5
	v_or_b32_e32 v8, s15, v12
	s_lshl_b32 s2, s3, 6
	v_mad_u64_u32 v[8:9], s[18:19], v8, s13, v[6:7]
	v_or_b32_e32 v7, s2, v7
	v_mad_i64_i32 v[10:11], s[18:19], v7, s12, 0
	v_or_b32_e32 v7, s2, v12
	v_bitop3_b32 v5, v12, 63, s15 bitop3:0xc8
	v_mad_i64_i32 v[12:13], s[18:19], v7, s12, 0
	v_or_b32_e32 v7, 0x200, v0
	v_lshrrev_b32_e32 v7, 4, v7
	v_lshl_add_u64 v[10:11], v[10:11], 1, s[6:7]
	v_lshlrev_b32_e32 v16, 1, v2
	v_mov_b32_e32 v17, 0
	v_xor_b32_e32 v9, v7, v0
	v_or_b32_e32 v7, s2, v7
	v_lshl_add_u64 v[10:11], v[10:11], 0, v[16:17]
	v_lshl_add_u64 v[12:13], v[12:13], 1, s[6:7]
	v_lshlrev_b32_e32 v16, 1, v6
	v_mad_i64_i32 v[14:15], s[18:19], v7, s12, 0
	v_lshlrev_b32_e32 v7, 4, v9
	v_lshl_add_u64 v[12:13], v[12:13], 0, v[16:17]
	v_and_b32_e32 v16, 0xf0, v7
	v_or_b32_e32 v7, 0x300, v0
	v_readfirstlane_b32 s25, v0
	v_lshrrev_b32_e32 v7, 4, v7
	s_lshr_b32 s24, s25, 6
	v_xor_b32_e32 v9, v7, v0
	v_or_b32_e32 v7, s2, v7
	v_lshl_add_u64 v[14:15], v[14:15], 1, s[6:7]
	v_mad_i64_i32 v[18:19], s[18:19], v7, s12, 0
	v_lshlrev_b32_e32 v7, 4, v9
	s_lshl_b32 s3, s24, 10
	v_lshl_add_u64 v[14:15], v[14:15], 0, v[16:17]
	v_lshl_add_u64 v[18:19], v[18:19], 1, s[6:7]
	v_and_b32_e32 v16, 0xf0, v7
	s_cmpk_lt_i32 s12, 0x80
	v_mov_b32_e32 v1, s20
	v_lshl_add_u64 v[16:17], v[18:19], 0, v[16:17]
	s_cselect_b64 s[18:19], -1, 0
	s_cmpk_gt_i32 s12, 0x7f
	s_mov_b32 s22, 0
	v_cmp_ne_u32_e64 s[20:21], s20, 0
	s_mov_b32 s23, 0
	s_mov_b32 s6, 0
	s_cbranch_scc0 .LBB11_2
	s_mul_i32 s6, s13, 0xffffffbf
	v_cmp_ne_u32_e32 vcc, 0, v3
	v_add_u32_e32 v7, s6, v4
	s_and_b64 vcc, s[20:21], vcc
	v_cndmask_b32_e32 v18, v2, v7, vcc
	v_mov_b32_e32 v7, s17
	v_mov_b32_e32 v9, s5
	v_mov_b32_e32 v22, s16
	v_mov_b32_e32 v23, s4
	v_cndmask_b32_e32 v21, v7, v9, vcc
	v_cndmask_b32_e32 v20, v22, v23, vcc
	v_ashrrev_i32_e32 v19, 31, v18
	s_mov_b32 m0, s3
	v_lshl_add_u64 v[18:19], v[18:19], 1, v[20:21]
	v_cmp_ne_u32_e32 vcc, 0, v5
	global_load_lds_dwordx4 v[18:19], off
	v_add_u32_e32 v18, s6, v8
	s_and_b64 vcc, s[20:21], vcc
	v_cndmask_b32_e32 v18, v6, v18, vcc
	v_cndmask_b32_e32 v21, v7, v9, vcc
	v_cndmask_b32_e32 v20, v22, v23, vcc
	v_ashrrev_i32_e32 v19, 31, v18
	v_lshl_add_u64 v[18:19], v[18:19], 1, v[20:21]
	s_add_i32 m0, s3, 0x1000
	s_nop 0
	global_load_lds_dwordx4 v[18:19], off
	s_add_i32 m0, s3, 0x2000
	s_nop 0
	global_load_lds_dwordx4 v[10:11], off
	s_add_i32 m0, s3, 0x3000
	s_nop 0
	global_load_lds_dwordx4 v[12:13], off
	s_add_i32 m0, s3, 0x4000
	s_nop 0
	global_load_lds_dwordx4 v[14:15], off
	s_add_i32 m0, s3, 0x5000
	s_cmpk_lt_i32 s13, 0x81
	global_load_lds_dwordx4 v[16:17], off
	s_cselect_b64 s[6:7], -1, 0
	v_cndmask_b32_e64 v7, 0, 1, s[6:7]
	s_and_b64 s[6:7], s[6:7], exec
	v_readfirstlane_b32 s22, v7
	s_cselect_b32 s23, 0, 0x80
	s_movk_i32 s6, 0x80
